# grid-barrier spin loops poll less often (s_sleep 8 instead of 1) to cut polling traffic while stragglers finish
# speedup vs baseline: 1.0357x; 1.0000x over previous
; __device__ __forceinline__ unsigned xb_ld(unsigned* p)              { return __hip_atomic_load(p, __ATOMIC_RELAXED, __HIP_MEMORY_SCOPE_AGENT); }
; __device__ __forceinline__ void xcd_barrier_complete(unsigned* bar, unsigned x, unsigned& nloc, unsigned& nx) {
;     const unsigned G = gridDim.x * gridDim.y * gridDim.z;
;     unsigned sum, cnt, mine, sp = 0u;
;     for (;;) {
;         sum = 0u; cnt = 0u; mine = 0u;
; #pragma unroll
;         for (unsigned j = 0; j < 16; ++j) { const unsigned c = xb_ld(&bar[XB_XCNT(j)]); sum += c; cnt += (c > 0u) ? 1u : 0u; mine = (j == x) ? c : mine; }
;         if (sum == G) break;
;         __builtin_amdgcn_s_sleep(1);
;         if ((++sp & 255u) == 0u) { if (xb_ld(&bar[XB_TMO])) break; if (sp > XB_SPIN_CAP) { atomicAdd(&bar[XB_TMO], 1u); break; } }
;     }
;     nloc = mine > 0u ? mine : 1u; nx = cnt > 0u ? cnt : 1u;
; }
.LBB0_77:
	global_load_dword v16, v17, s[90:91] offset:1024 sc1
	global_load_dword v1, v17, s[90:91] offset:1280 sc1
	global_load_dword v2, v17, s[90:91] offset:1536 sc1
	global_load_dword v3, v17, s[90:91] offset:1792 sc1
	global_load_dword v4, v17, s[90:91] offset:2048 sc1
	global_load_dword v5, v17, s[90:91] offset:2304 sc1
	global_load_dword v6, v17, s[90:91] offset:2560 sc1
	global_load_dword v7, v17, s[90:91] offset:2816 sc1
	global_load_dword v8, v17, s[90:91] offset:3072 sc1
	global_load_dword v9, v17, s[90:91] offset:3328 sc1
	global_load_dword v10, v17, s[90:91] offset:3584 sc1
	global_load_dword v11, v17, s[90:91] offset:3840 sc1
	global_load_dword v12, v17, s[6:7] sc1
	global_load_dword v13, v17, s[8:9] sc1
	global_load_dword v14, v17, s[10:11] sc1
	global_load_dword v15, v17, s[12:13] sc1
	s_mov_b64 s[14:15], -1
	s_mov_b64 s[16:17], -1
	s_waitcnt vmcnt(14)
	v_add_u32_e32 v18, v1, v16
	s_waitcnt vmcnt(13)
	v_add_u32_e32 v18, v18, v2
	s_waitcnt vmcnt(12)
	v_add_u32_e32 v18, v18, v3
	s_waitcnt vmcnt(11)
	v_add_u32_e32 v18, v18, v4
	s_waitcnt vmcnt(10)
	v_add_u32_e32 v18, v18, v5
	s_waitcnt vmcnt(9)
	v_add_u32_e32 v18, v18, v6
	s_waitcnt vmcnt(8)
	v_add_u32_e32 v18, v18, v7
	s_waitcnt vmcnt(7)
	v_add_u32_e32 v18, v18, v8
	s_waitcnt vmcnt(6)
	v_add_u32_e32 v18, v18, v9
	s_waitcnt vmcnt(5)
	v_add_u32_e32 v18, v18, v10
	s_waitcnt vmcnt(4)
	v_add_u32_e32 v18, v18, v11
	s_waitcnt vmcnt(3)
	v_add_u32_e32 v18, v18, v12
	s_waitcnt vmcnt(2)
	v_add_u32_e32 v18, v18, v13
	s_waitcnt vmcnt(1)
	v_add_u32_e32 v18, v18, v14
	s_waitcnt vmcnt(0)
	v_add_u32_e32 v18, v18, v15
	v_cmp_eq_u32_e32 vcc, s3, v18
	s_cbranch_vccnz .LBB0_76
	s_and_b32 s5, s4, 0xff
	s_cmp_eq_u32 s5, 0
	s_mov_b64 s[18:19], -1
	s_sleep 8
	s_cbranch_scc0 .LBB0_81
	global_load_dword v18, v17, s[90:91] offset:512 sc1
	s_waitcnt vmcnt(0)
	v_cmp_eq_u32_e32 vcc, 0, v18
	s_cbranch_vccnz .LBB0_83
	s_mov_b64 s[18:19], 0

; __device__ __forceinline__ unsigned xb_ld(unsigned* p)              { return __hip_atomic_load(p, __ATOMIC_RELAXED, __HIP_MEMORY_SCOPE_AGENT); }
; __device__ __forceinline__ unsigned xb_add(unsigned* p, unsigned v) { return __hip_atomic_fetch_add(p, v, __ATOMIC_RELAXED, __HIP_MEMORY_SCOPE_AGENT); }
; #define XB_SPIN(cond, bar) do { unsigned _sp = 0; while (cond) { __builtin_amdgcn_s_sleep(1); \
;     if ((++_sp & 255u) == 0u) { if (xb_ld(&(bar)[XB_TMO])) break; if (_sp > XB_SPIN_CAP) { atomicAdd(&(bar)[XB_TMO], 1u); break; } } } } while (0)
; __device__ __forceinline__ void xcd_barrier(const XcdBarrier& b) {
;     ...
;             const unsigned og = xb_add(&bar[XB_TOP], 1u);
;             const unsigned tg = og / nx;
;             if (og + 1u == (tg + 1u) * nx) xb_add(&bar[XB_TOPGEN], 1u);
;             else XB_SPIN(xb_ld(&bar[XB_TOPGEN]) == tg, bar);
.LBB0_95:
	s_and_b32 s4, s3, 0xff
	s_mov_b64 s[18:19], -1
	s_cmp_lg_u32 s4, 0
	s_mov_b64 s[22:23], -1
	s_sleep 8
	s_cbranch_scc1 .LBB0_98
	global_load_dword v3, v1, s[90:91] offset:512 sc1
	s_waitcnt vmcnt(0)
	v_cmp_eq_u32_e32 vcc, 0, v3
	s_cbranch_vccnz .LBB0_100
	s_mov_b64 s[22:23], 0
	s_mov_b64 s[20:21], -1

; __device__ __forceinline__ unsigned xb_ld(unsigned* p)              { return __hip_atomic_load(p, __ATOMIC_RELAXED, __HIP_MEMORY_SCOPE_AGENT); }
; #define XB_SPIN(cond, bar) do { unsigned _sp = 0; while (cond) { __builtin_amdgcn_s_sleep(1); \
;     if ((++_sp & 255u) == 0u) { if (xb_ld(&(bar)[XB_TMO])) break; if (_sp > XB_SPIN_CAP) { atomicAdd(&(bar)[XB_TMO], 1u); break; } } } } while (0)
; __device__ __forceinline__ void xcd_barrier(const XcdBarrier& b) {
;     ...
;             XB_SPIN(xb_ld(&bar[XB_XGEN(b.x)]) == gen, bar);
.LBB0_112:
	s_and_b32 s4, s3, 0xff
	s_cmp_lg_u32 s4, 0
	s_mov_b64 s[22:23], -1
	s_sleep 8
	s_cbranch_scc1 .LBB0_115
	global_load_dword v2, v1, s[12:13] sc1
	s_waitcnt vmcnt(0)
	v_cmp_eq_u32_e32 vcc, 0, v2
	s_cbranch_vccnz .LBB0_117
	s_mov_b64 s[22:23], 0
	s_mov_b64 s[20:21], -1

; __device__ __forceinline__ unsigned xb_ld(unsigned* p)              { return __hip_atomic_load(p, __ATOMIC_RELAXED, __HIP_MEMORY_SCOPE_AGENT); }
; __device__ __forceinline__ void xcd_barrier_complete(unsigned* bar, unsigned x, unsigned& nloc, unsigned& nx) {
;     const unsigned G = gridDim.x * gridDim.y * gridDim.z;
;     unsigned sum, cnt, mine, sp = 0u;
;     for (;;) {
;         sum = 0u; cnt = 0u; mine = 0u;
; #pragma unroll
;         for (unsigned j = 0; j < 16; ++j) { const unsigned c = xb_ld(&bar[XB_XCNT(j)]); sum += c; cnt += (c > 0u) ? 1u : 0u; mine = (j == x) ? c : mine; }
;         if (sum == G) break;
;         __builtin_amdgcn_s_sleep(1);
;         if ((++sp & 255u) == 0u) { if (xb_ld(&bar[XB_TMO])) break; if (sp > XB_SPIN_CAP) { atomicAdd(&bar[XB_TMO], 1u); break; } }
;     }
;     nloc = mine > 0u ? mine : 1u; nx = cnt > 0u ? cnt : 1u;
; }
.LBB0_602:
	global_load_dword v16, v17, s[90:91] offset:1024 sc1
	global_load_dword v1, v17, s[90:91] offset:1280 sc1
	global_load_dword v2, v17, s[90:91] offset:1536 sc1
	global_load_dword v3, v17, s[90:91] offset:1792 sc1
	global_load_dword v4, v17, s[90:91] offset:2048 sc1
	global_load_dword v5, v17, s[90:91] offset:2304 sc1
	global_load_dword v6, v17, s[90:91] offset:2560 sc1
	global_load_dword v7, v17, s[90:91] offset:2816 sc1
	global_load_dword v8, v17, s[90:91] offset:3072 sc1
	global_load_dword v9, v17, s[90:91] offset:3328 sc1
	global_load_dword v10, v17, s[90:91] offset:3584 sc1
	global_load_dword v11, v17, s[90:91] offset:3840 sc1
	global_load_dword v12, v17, s[8:9] sc1
	global_load_dword v13, v17, s[10:11] sc1
	global_load_dword v14, v17, s[12:13] sc1
	global_load_dword v15, v17, s[14:15] sc1
	s_mov_b64 s[16:17], -1
	s_mov_b64 s[18:19], -1
	s_waitcnt vmcnt(14)
	v_add_u32_e32 v18, v1, v16
	s_waitcnt vmcnt(13)
	v_add_u32_e32 v18, v18, v2
	s_waitcnt vmcnt(12)
	v_add_u32_e32 v18, v18, v3
	s_waitcnt vmcnt(11)
	v_add_u32_e32 v18, v18, v4
	s_waitcnt vmcnt(10)
	v_add_u32_e32 v18, v18, v5
	s_waitcnt vmcnt(9)
	v_add_u32_e32 v18, v18, v6
	s_waitcnt vmcnt(8)
	v_add_u32_e32 v18, v18, v7
	s_waitcnt vmcnt(7)
	v_add_u32_e32 v18, v18, v8
	s_waitcnt vmcnt(6)
	v_add_u32_e32 v18, v18, v9
	s_waitcnt vmcnt(5)
	v_add_u32_e32 v18, v18, v10
	s_waitcnt vmcnt(4)
	v_add_u32_e32 v18, v18, v11
	s_waitcnt vmcnt(3)
	v_add_u32_e32 v18, v18, v12
	s_waitcnt vmcnt(2)
	v_add_u32_e32 v18, v18, v13
	s_waitcnt vmcnt(1)
	v_add_u32_e32 v18, v18, v14
	s_waitcnt vmcnt(0)
	v_add_u32_e32 v18, v18, v15
	v_cmp_eq_u32_e32 vcc, s3, v18
	s_cbranch_vccnz .LBB0_601
	s_and_b32 s5, s4, 0xff
	s_cmp_eq_u32 s5, 0
	s_mov_b64 s[20:21], -1
	s_sleep 8
	s_cbranch_scc0 .LBB0_606
	global_load_dword v18, v17, s[90:91] offset:512 sc1
	s_waitcnt vmcnt(0)
	v_cmp_eq_u32_e32 vcc, 0, v18
	s_cbranch_vccnz .LBB0_608
	s_mov_b64 s[20:21], 0

; __device__ __forceinline__ unsigned xb_ld(unsigned* p)              { return __hip_atomic_load(p, __ATOMIC_RELAXED, __HIP_MEMORY_SCOPE_AGENT); }
; __device__ __forceinline__ unsigned xb_add(unsigned* p, unsigned v) { return __hip_atomic_fetch_add(p, v, __ATOMIC_RELAXED, __HIP_MEMORY_SCOPE_AGENT); }
; #define XB_SPIN(cond, bar) do { unsigned _sp = 0; while (cond) { __builtin_amdgcn_s_sleep(1); \
;     if ((++_sp & 255u) == 0u) { if (xb_ld(&(bar)[XB_TMO])) break; if (_sp > XB_SPIN_CAP) { atomicAdd(&(bar)[XB_TMO], 1u); break; } } } } while (0)
; __device__ __forceinline__ void xcd_barrier(const XcdBarrier& b) {
;     ...
;             const unsigned og = xb_add(&bar[XB_TOP], 1u);
;             const unsigned tg = og / nx;
;             if (og + 1u == (tg + 1u) * nx) xb_add(&bar[XB_TOPGEN], 1u);
;             else XB_SPIN(xb_ld(&bar[XB_TOPGEN]) == tg, bar);
.LBB0_620:
	s_and_b32 s4, s3, 0xff
	s_mov_b64 s[20:21], -1
	s_cmp_lg_u32 s4, 0
	s_mov_b64 s[26:27], -1
	s_sleep 8
	s_cbranch_scc1 .LBB0_623
	global_load_dword v3, v1, s[90:91] offset:512 sc1
	s_waitcnt vmcnt(0)
	v_cmp_eq_u32_e32 vcc, 0, v3
	s_cbranch_vccnz .LBB0_625
	s_mov_b64 s[26:27], 0
	s_mov_b64 s[22:23], -1

; __device__ __forceinline__ unsigned xb_ld(unsigned* p)              { return __hip_atomic_load(p, __ATOMIC_RELAXED, __HIP_MEMORY_SCOPE_AGENT); }
; #define XB_SPIN(cond, bar) do { unsigned _sp = 0; while (cond) { __builtin_amdgcn_s_sleep(1); \
;     if ((++_sp & 255u) == 0u) { if (xb_ld(&(bar)[XB_TMO])) break; if (_sp > XB_SPIN_CAP) { atomicAdd(&(bar)[XB_TMO], 1u); break; } } } } while (0)
; __device__ __forceinline__ void xcd_barrier(const XcdBarrier& b) {
;     ...
;             XB_SPIN(xb_ld(&bar[XB_XGEN(b.x)]) == gen, bar);
.LBB0_637:
	s_and_b32 s4, s3, 0xff
	s_cmp_lg_u32 s4, 0
	s_mov_b64 s[26:27], -1
	s_sleep 8
	s_cbranch_scc1 .LBB0_640
	global_load_dword v2, v1, s[14:15] sc1
	s_waitcnt vmcnt(0)
	v_cmp_eq_u32_e32 vcc, 0, v2
	s_cbranch_vccnz .LBB0_642
	s_mov_b64 s[26:27], 0
	s_mov_b64 s[22:23], -1

; __device__ __forceinline__ unsigned xb_ld(unsigned* p)              { return __hip_atomic_load(p, __ATOMIC_RELAXED, __HIP_MEMORY_SCOPE_AGENT); }
; __device__ __forceinline__ void xcd_barrier_complete(unsigned* bar, unsigned x, unsigned& nloc, unsigned& nx) {
;     const unsigned G = gridDim.x * gridDim.y * gridDim.z;
;     unsigned sum, cnt, mine, sp = 0u;
;     for (;;) {
;         sum = 0u; cnt = 0u; mine = 0u;
; #pragma unroll
;         for (unsigned j = 0; j < 16; ++j) { const unsigned c = xb_ld(&bar[XB_XCNT(j)]); sum += c; cnt += (c > 0u) ? 1u : 0u; mine = (j == x) ? c : mine; }
;         if (sum == G) break;
;         __builtin_amdgcn_s_sleep(1);
;         if ((++sp & 255u) == 0u) { if (xb_ld(&bar[XB_TMO])) break; if (sp > XB_SPIN_CAP) { atomicAdd(&bar[XB_TMO], 1u); break; } }
;     }
;     nloc = mine > 0u ? mine : 1u; nx = cnt > 0u ? cnt : 1u;
; }
.LBB0_1108:
	global_load_dword v17, v18, s[90:91] offset:1024 sc1
	global_load_dword v2, v18, s[90:91] offset:1280 sc1
	global_load_dword v3, v18, s[90:91] offset:1536 sc1
	global_load_dword v4, v18, s[90:91] offset:1792 sc1
	global_load_dword v5, v18, s[90:91] offset:2048 sc1
	global_load_dword v6, v18, s[90:91] offset:2304 sc1
	global_load_dword v7, v18, s[90:91] offset:2560 sc1
	global_load_dword v8, v18, s[90:91] offset:2816 sc1
	global_load_dword v9, v18, s[90:91] offset:3072 sc1
	global_load_dword v10, v18, s[90:91] offset:3328 sc1
	global_load_dword v11, v18, s[90:91] offset:3584 sc1
	global_load_dword v12, v18, s[90:91] offset:3840 sc1
	global_load_dword v13, v18, s[6:7] sc1
	global_load_dword v14, v18, s[8:9] sc1
	global_load_dword v15, v18, s[10:11] sc1
	global_load_dword v16, v18, s[12:13] sc1
	s_mov_b64 s[14:15], -1
	s_mov_b64 s[16:17], -1
	s_waitcnt vmcnt(14)
	v_add_u32_e32 v19, v2, v17
	s_waitcnt vmcnt(13)
	v_add_u32_e32 v19, v19, v3
	s_waitcnt vmcnt(12)
	v_add_u32_e32 v19, v19, v4
	s_waitcnt vmcnt(11)
	v_add_u32_e32 v19, v19, v5
	s_waitcnt vmcnt(10)
	v_add_u32_e32 v19, v19, v6
	s_waitcnt vmcnt(9)
	v_add_u32_e32 v19, v19, v7
	s_waitcnt vmcnt(8)
	v_add_u32_e32 v19, v19, v8
	s_waitcnt vmcnt(7)
	v_add_u32_e32 v19, v19, v9
	s_waitcnt vmcnt(6)
	v_add_u32_e32 v19, v19, v10
	s_waitcnt vmcnt(5)
	v_add_u32_e32 v19, v19, v11
	s_waitcnt vmcnt(4)
	v_add_u32_e32 v19, v19, v12
	s_waitcnt vmcnt(3)
	v_add_u32_e32 v19, v19, v13
	s_waitcnt vmcnt(2)
	v_add_u32_e32 v19, v19, v14
	s_waitcnt vmcnt(1)
	v_add_u32_e32 v19, v19, v15
	s_waitcnt vmcnt(0)
	v_add_u32_e32 v19, v19, v16
	v_cmp_eq_u32_e32 vcc, s3, v19
	s_cbranch_vccnz .LBB0_1107
	s_and_b32 s5, s4, 0xff
	s_cmp_eq_u32 s5, 0
	s_mov_b64 s[18:19], -1
	s_sleep 8
	s_cbranch_scc0 .LBB0_1112
	global_load_dword v19, v18, s[90:91] offset:512 sc1
	s_waitcnt vmcnt(0)
	v_cmp_eq_u32_e32 vcc, 0, v19
	s_cbranch_vccnz .LBB0_1114
	s_mov_b64 s[18:19], 0

; __device__ __forceinline__ unsigned xb_ld(unsigned* p)              { return __hip_atomic_load(p, __ATOMIC_RELAXED, __HIP_MEMORY_SCOPE_AGENT); }
; __device__ __forceinline__ unsigned xb_add(unsigned* p, unsigned v) { return __hip_atomic_fetch_add(p, v, __ATOMIC_RELAXED, __HIP_MEMORY_SCOPE_AGENT); }
; #define XB_SPIN(cond, bar) do { unsigned _sp = 0; while (cond) { __builtin_amdgcn_s_sleep(1); \
;     if ((++_sp & 255u) == 0u) { if (xb_ld(&(bar)[XB_TMO])) break; if (_sp > XB_SPIN_CAP) { atomicAdd(&(bar)[XB_TMO], 1u); break; } } } } while (0)
; __device__ __forceinline__ void xcd_barrier(const XcdBarrier& b) {
;     ...
;             const unsigned og = xb_add(&bar[XB_TOP], 1u);
;             const unsigned tg = og / nx;
;             if (og + 1u == (tg + 1u) * nx) xb_add(&bar[XB_TOPGEN], 1u);
;             else XB_SPIN(xb_ld(&bar[XB_TOPGEN]) == tg, bar);
.LBB0_1126:
	s_and_b32 s4, s3, 0xff
	s_mov_b64 s[18:19], -1
	s_cmp_lg_u32 s4, 0
	s_mov_b64 s[22:23], -1
	s_sleep 8
	s_cbranch_scc1 .LBB0_1129
	global_load_dword v4, v2, s[90:91] offset:512 sc1
	s_waitcnt vmcnt(0)
	v_cmp_eq_u32_e32 vcc, 0, v4
	s_cbranch_vccnz .LBB0_1131
	s_mov_b64 s[22:23], 0
	s_mov_b64 s[20:21], -1

; __device__ __forceinline__ unsigned xb_ld(unsigned* p)              { return __hip_atomic_load(p, __ATOMIC_RELAXED, __HIP_MEMORY_SCOPE_AGENT); }
; #define XB_SPIN(cond, bar) do { unsigned _sp = 0; while (cond) { __builtin_amdgcn_s_sleep(1); \
;     if ((++_sp & 255u) == 0u) { if (xb_ld(&(bar)[XB_TMO])) break; if (_sp > XB_SPIN_CAP) { atomicAdd(&(bar)[XB_TMO], 1u); break; } } } } while (0)
; __device__ __forceinline__ void xcd_barrier(const XcdBarrier& b) {
;     ...
;             XB_SPIN(xb_ld(&bar[XB_XGEN(b.x)]) == gen, bar);
.LBB0_1143:
	s_and_b32 s4, s3, 0xff
	s_cmp_lg_u32 s4, 0
	s_mov_b64 s[22:23], -1
	s_sleep 8
	s_cbranch_scc1 .LBB0_1146
	global_load_dword v3, v2, s[12:13] sc1
	s_waitcnt vmcnt(0)
	v_cmp_eq_u32_e32 vcc, 0, v3
	s_cbranch_vccnz .LBB0_1148
	s_mov_b64 s[22:23], 0
	s_mov_b64 s[20:21], -1

; __device__ __forceinline__ unsigned xb_ld(unsigned* p)              { return __hip_atomic_load(p, __ATOMIC_RELAXED, __HIP_MEMORY_SCOPE_AGENT); }
; __device__ __forceinline__ void xcd_barrier_complete(unsigned* bar, unsigned x, unsigned& nloc, unsigned& nx) {
;     const unsigned G = gridDim.x * gridDim.y * gridDim.z;
;     unsigned sum, cnt, mine, sp = 0u;
;     for (;;) {
;         sum = 0u; cnt = 0u; mine = 0u;
; #pragma unroll
;         for (unsigned j = 0; j < 16; ++j) { const unsigned c = xb_ld(&bar[XB_XCNT(j)]); sum += c; cnt += (c > 0u) ? 1u : 0u; mine = (j == x) ? c : mine; }
;         if (sum == G) break;
;         __builtin_amdgcn_s_sleep(1);
;         if ((++sp & 255u) == 0u) { if (xb_ld(&bar[XB_TMO])) break; if (sp > XB_SPIN_CAP) { atomicAdd(&bar[XB_TMO], 1u); break; } }
;     }
;     nloc = mine > 0u ? mine : 1u; nx = cnt > 0u ? cnt : 1u;
; }
.LBB0_1241:
	global_load_dword v16, v17, s[90:91] offset:1024 sc1
	global_load_dword v1, v17, s[90:91] offset:1280 sc1
	global_load_dword v2, v17, s[90:91] offset:1536 sc1
	global_load_dword v3, v17, s[90:91] offset:1792 sc1
	global_load_dword v4, v17, s[90:91] offset:2048 sc1
	global_load_dword v5, v17, s[90:91] offset:2304 sc1
	global_load_dword v6, v17, s[90:91] offset:2560 sc1
	global_load_dword v7, v17, s[90:91] offset:2816 sc1
	global_load_dword v8, v17, s[90:91] offset:3072 sc1
	global_load_dword v9, v17, s[90:91] offset:3328 sc1
	global_load_dword v10, v17, s[90:91] offset:3584 sc1
	global_load_dword v11, v17, s[90:91] offset:3840 sc1
	global_load_dword v12, v17, s[2:3] sc1
	global_load_dword v13, v17, s[4:5] sc1
	global_load_dword v14, v17, s[6:7] sc1
	global_load_dword v15, v17, s[8:9] sc1
	s_mov_b64 s[10:11], -1
	s_mov_b64 s[12:13], -1
	s_waitcnt vmcnt(14)
	v_add_u32_e32 v18, v1, v16
	s_waitcnt vmcnt(13)
	v_add_u32_e32 v18, v18, v2
	s_waitcnt vmcnt(12)
	v_add_u32_e32 v18, v18, v3
	s_waitcnt vmcnt(11)
	v_add_u32_e32 v18, v18, v4
	s_waitcnt vmcnt(10)
	v_add_u32_e32 v18, v18, v5
	s_waitcnt vmcnt(9)
	v_add_u32_e32 v18, v18, v6
	s_waitcnt vmcnt(8)
	v_add_u32_e32 v18, v18, v7
	s_waitcnt vmcnt(7)
	v_add_u32_e32 v18, v18, v8
	s_waitcnt vmcnt(6)
	v_add_u32_e32 v18, v18, v9
	s_waitcnt vmcnt(5)
	v_add_u32_e32 v18, v18, v10
	s_waitcnt vmcnt(4)
	v_add_u32_e32 v18, v18, v11
	s_waitcnt vmcnt(3)
	v_add_u32_e32 v18, v18, v12
	s_waitcnt vmcnt(2)
	v_add_u32_e32 v18, v18, v13
	s_waitcnt vmcnt(1)
	v_add_u32_e32 v18, v18, v14
	s_waitcnt vmcnt(0)
	v_add_u32_e32 v18, v18, v15
	v_cmp_eq_u32_e32 vcc, s16, v18
	s_cbranch_vccnz .LBB0_1240
	s_and_b32 s10, s17, 0xff
	s_cmp_eq_u32 s10, 0
	s_mov_b64 s[10:11], -1
	s_mov_b64 s[14:15], -1
	s_sleep 8
	s_cbranch_scc0 .LBB0_1245
	global_load_dword v18, v17, s[90:91] offset:512 sc1
	s_waitcnt vmcnt(0)
	v_cmp_eq_u32_e32 vcc, 0, v18
	s_cbranch_vccnz .LBB0_1247
	s_mov_b64 s[14:15], 0

; __device__ __forceinline__ unsigned xb_ld(unsigned* p)              { return __hip_atomic_load(p, __ATOMIC_RELAXED, __HIP_MEMORY_SCOPE_AGENT); }
; __device__ __forceinline__ unsigned xb_add(unsigned* p, unsigned v) { return __hip_atomic_fetch_add(p, v, __ATOMIC_RELAXED, __HIP_MEMORY_SCOPE_AGENT); }
; #define XB_SPIN(cond, bar) do { unsigned _sp = 0; while (cond) { __builtin_amdgcn_s_sleep(1); \
;     if ((++_sp & 255u) == 0u) { if (xb_ld(&(bar)[XB_TMO])) break; if (_sp > XB_SPIN_CAP) { atomicAdd(&(bar)[XB_TMO], 1u); break; } } } } while (0)
; __device__ __forceinline__ void xcd_barrier(const XcdBarrier& b) {
;     ...
;             const unsigned og = xb_add(&bar[XB_TOP], 1u);
;             const unsigned tg = og / nx;
;             if (og + 1u == (tg + 1u) * nx) xb_add(&bar[XB_TOPGEN], 1u);
;             else XB_SPIN(xb_ld(&bar[XB_TOPGEN]) == tg, bar);
.LBB0_1259:
	s_and_b32 s16, s20, 0xff
	s_mov_b64 s[14:15], -1
	s_cmp_lg_u32 s16, 0
	s_mov_b64 s[18:19], -1
	s_sleep 8
	s_cbranch_scc1 .LBB0_1262
	global_load_dword v3, v1, s[90:91] offset:512 sc1
	s_waitcnt vmcnt(0)
	v_cmp_eq_u32_e32 vcc, 0, v3
	s_cbranch_vccnz .LBB0_1264
	s_mov_b64 s[18:19], 0
	s_mov_b64 s[16:17], -1

; __device__ __forceinline__ unsigned xb_ld(unsigned* p)              { return __hip_atomic_load(p, __ATOMIC_RELAXED, __HIP_MEMORY_SCOPE_AGENT); }
; #define XB_SPIN(cond, bar) do { unsigned _sp = 0; while (cond) { __builtin_amdgcn_s_sleep(1); \
;     if ((++_sp & 255u) == 0u) { if (xb_ld(&(bar)[XB_TMO])) break; if (_sp > XB_SPIN_CAP) { atomicAdd(&(bar)[XB_TMO], 1u); break; } } } } while (0)
; __device__ __forceinline__ void xcd_barrier(const XcdBarrier& b) {
;     ...
;             XB_SPIN(xb_ld(&bar[XB_XGEN(b.x)]) == gen, bar);
.LBB0_1276:
	s_and_b32 s16, s22, 0xff
	s_cmp_lg_u32 s16, 0
	s_mov_b64 s[18:19], -1
	s_sleep 8
	s_cbranch_scc1 .LBB0_1279
	global_load_dword v2, v1, s[8:9] sc1
	s_waitcnt vmcnt(0)
	v_cmp_eq_u32_e32 vcc, 0, v2
	s_cbranch_vccnz .LBB0_1281
	s_mov_b64 s[18:19], 0
	s_mov_b64 s[16:17], -1
